# baseline (speedup 1.0000x reference)
.LBB3_9:
	s_nop 1
	v_exp_f32_e32 v93, v50
	v_exp_f32_e32 v94, v51
	v_exp_f32_e32 v95, v52
	v_exp_f32_e32 v35, v66
	v_exp_f32_e32 v96, v53
	v_exp_f32_e32 v90, v67
	v_add_f32_e32 v36, 0, v93
	v_exp_f32_e32 v91, v68
	v_add_f32_e32 v36, v36, v94
	v_exp_f32_e32 v92, v69
	v_add_f32_e32 v36, v36, v95
	v_exp_f32_e32 v66, v70
	v_add_f32_e32 v37, v36, v96
	v_exp_f32_e32 v67, v54
	v_add_f32_e32 v36, 0, v35
	v_exp_f32_e32 v68, v71
	v_exp_f32_e32 v69, v55
	v_add_f32_e32 v36, v36, v90
	v_exp_f32_e32 v70, v72
	v_exp_f32_e32 v71, v56
	v_add_f32_e32 v36, v36, v91
	v_exp_f32_e32 v72, v73
	v_exp_f32_e32 v73, v57
	v_add_f32_e32 v36, v36, v92
	v_exp_f32_e32 v74, v74
	v_exp_f32_e32 v82, v75
	v_exp_f32_e32 v75, v58
	v_add_f32_e32 v36, v36, v66
	v_add_f32_e32 v37, v37, v67
	v_exp_f32_e32 v83, v59
	v_add_f32_e32 v36, v36, v68
	v_add_f32_e32 v37, v37, v69
	v_exp_f32_e32 v76, v76
	v_exp_f32_e32 v84, v77
	v_exp_f32_e32 v77, v60
	v_add_f32_e32 v36, v36, v70
	v_add_f32_e32 v37, v37, v71
	v_exp_f32_e32 v85, v61
	v_add_f32_e32 v36, v36, v72
	v_add_f32_e32 v37, v37, v73
	v_exp_f32_e32 v78, v78
	v_exp_f32_e32 v86, v79
	v_exp_f32_e32 v79, v62
	v_add_f32_e32 v36, v36, v74
	v_add_f32_e32 v37, v37, v75
	v_exp_f32_e32 v87, v63
	v_add_f32_e32 v36, v36, v82
	v_add_f32_e32 v37, v37, v83
	v_add_u32_e32 v56, s4, v109
	v_add_f32_e32 v36, v36, v76
	v_add_f32_e32 v37, v37, v77
	v_exp_f32_e32 v80, v80
	v_exp_f32_e32 v88, v81
	v_exp_f32_e32 v81, v64
	v_add_f32_e32 v36, v36, v84
	v_add_f32_e32 v37, v37, v85
	v_add_u32_e32 v40, v56, v110
	v_add_u32_e32 v48, v56, v112
	v_exp_f32_e32 v89, v65
	v_add_f32_e32 v52, v36, v78
	v_add_f32_e32 v53, v37, v79
	ds_read_b128 v[36:39], v40 offset:8192
	ds_read_b128 v[40:43], v40 offset:12288
	ds_read_b128 v[44:47], v48 offset:8192
	ds_read_b128 v[48:51], v48 offset:12288
	v_add_f32_e32 v52, v52, v86
	v_add_f32_e32 v53, v53, v87
	s_nop 0
	v_add_f32_e32 v52, v52, v80
	v_add_f32_e32 v53, v53, v81
	s_nop 0
	v_add_f32_e32 v52, v52, v88
	v_add_f32_e32 v53, v53, v89
	s_nop 0
	v_add_f32_e32 v60, v52, v53
	v_cvt_pk_f16_f32 v55, v70, v72
	v_cvt_pk_f16_f32 v54, v66, v68
	v_cvt_pk_f16_f32 v53, v91, v92
	v_cvt_pk_f16_f32 v52, v35, v90
	v_add_u32_e32 v35, v56, v111
	s_waitcnt lgkmcnt(0)
	v_mfma_f32_32x32x16_f16 v[18:33], v[36:39], v[52:55], v[18:33]
	v_cvt_pk_f16_f32 v39, v80, v88
	v_cvt_pk_f16_f32 v38, v78, v86
	v_cvt_pk_f16_f32 v37, v76, v84
	v_cvt_pk_f16_f32 v36, v74, v82
	v_mfma_f32_32x32x16_f16 v[2:17], v[40:43], v[52:55], v[2:17]
	s_nop 0
	v_mfma_f32_32x32x16_f16 v[18:33], v[44:47], v[36:39], v[18:33]
	ds_read_b128 v[40:43], v35 offset:8192
	ds_read_b128 v[44:47], v35 offset:12288
	v_add_u32_e32 v35, v56, v113
	ds_read_b128 v[52:55], v35 offset:8192
	ds_read_b128 v[56:59], v35 offset:12288
	v_mfma_f32_32x32x16_f16 v[2:17], v[48:51], v[36:39], v[2:17]
	v_cvt_pk_f16_f32 v39, v71, v73
	v_cvt_pk_f16_f32 v38, v67, v69
	v_cvt_pk_f16_f32 v37, v95, v96
	v_cvt_pk_f16_f32 v36, v93, v94
	v_add_f32_e32 v35, v114, v60
	v_cmp_gt_u32_e32 vcc, 32, v99
	s_waitcnt lgkmcnt(0)
	v_mfma_f32_32x32x16_f16 v[18:33], v[40:43], v[36:39], v[18:33]
	v_mov_b32_e32 v40, v35
	s_nop 1
	v_permlane32_swap_b32_e32 v35, v40
	v_add_f32_e32 v35, v35, v40
	v_mfma_f32_32x32x16_f16 v[2:17], v[44:47], v[36:39], v[2:17]
	v_cvt_pk_f16_f32 v39, v81, v89
	v_cvt_pk_f16_f32 v38, v79, v87
	v_cvt_pk_f16_f32 v37, v77, v85
	v_cvt_pk_f16_f32 v36, v75, v83
	s_nop 1
	v_mfma_f32_32x32x16_f16 v[18:33], v[52:55], v[36:39], v[18:33]
	v_mfma_f32_32x32x16_f16 v[2:17], v[56:59], v[36:39], v[2:17]
	s_and_saveexec_b64 s[4:5], vcc
	s_cbranch_execz .LBB3_11
	s_mul_i32 s6, s20, 24
	s_add_u32 s6, s6, s12
	s_addc_u32 s7, 0, s13
	s_lshl_b64 s[6:7], s[6:7], 14
	s_add_u32 s6, s0, s6
	s_addc_u32 s7, s1, s7
	s_lshl_b64 s[0:1], s[2:3], 3
	s_add_u32 s0, s6, s0
	v_xor_b32_e32 v34, 0x80000000, v34
	s_addc_u32 s1, s7, s1
	v_lshlrev_b32_e32 v36, 3, v98
	global_store_dwordx2 v36, v[34:35], s[0:1] sc1 nt
